# c5
# speedup vs baseline: 1.0018x; 1.0018x over previous
.LBB6_148:
	s_or_b64 exec, exec, s[16:17]
	v_add_f32_e32 v212, v45, v9
	v_mov_b32_e32 v45, v43
	v_mov_b32_e32 v9, v7
	v_pk_add_f32 v[166:167], v[44:45], v[8:9]
	s_add_i32 s16, s3, s33
	s_bfe_u32 s42, s16, 0x30003
	s_bfe_u32 s43, s16, 0x20001
	v_lshl_or_b32 v6, s42, 2, v190
	s_lshl_b32 s16, s43, 3
	v_add_u32_e32 v6, v6, v198
	s_add_i32 s16, s16, s62
	v_lshl_add_u32 v6, v6, 5, s16
	v_add_lshl_u32 v6, v6, v197, 12
	v_lshlrev_b32_e32 v7, 2, v206
	s_movk_i32 s16, 0x200
	v_or3_b32 v174, v6, v7, s16
	v_mov_b32_e32 v175, 0
	v_lshl_add_u64 v[6:7], s[28:29], 0, v[174:175]
	s_mov_b64 s[16:17], 0x3680
	v_lshl_add_u64 v[176:177], v[6:7], 0, s[16:17]
	s_lshl_b32 s16, s59, 20
	s_lshl_b32 s17, s42, 17
	s_or_b32 s16, s16, s17
	v_lshl_add_u32 v6, v207, 15, s16
	s_lshl_b32 s17, s43, 13
	v_or_b32_e32 v6, s17, v6
	v_add_u32_e32 v7, v205, v204
	v_lshl_add_u32 v204, v7, 10, v6
	v_lshl_add_u32 v6, v181, 15, s16
	v_or_b32_e32 v6, s17, v6
	v_add_u32_e32 v7, v180, v191
	v_lshl_add_u32 v205, v7, 10, v6
	v_lshl_add_u32 v6, v179, 15, s16
	v_or_b32_e32 v6, s17, v6
	v_add_u32_e32 v7, v208, v178
	v_lshl_add_u32 v207, v7, 10, v6
	v_lshl_or_b32 v6, v184, 15, s16
	v_or_b32_e32 v6, s17, v6
	v_add_u32_e32 v7, v183, v191
	s_mov_b32 s63, 2
	v_lshl_add_u32 v208, v7, 10, v6
	s_mov_b64 s[42:43], 0x100
	s_waitcnt lgkmcnt(0)
	v_mbcnt_lo_u32_b32 v242, -1, 0
	v_mbcnt_hi_u32_b32 v242, -1, v242
	v_and_b32_e32 v242, 31, v242
	v_cmp_eq_u32_e64 s[66:67], 0, v242
	v_cmp_eq_u32_e64 s[68:69], 31, v242
	v_mul_u32_u24_e32 v243, 11, v242
	v_lshrrev_b32_e32 v243, 5, v243
	v_mul_u32_u24_e32 v243, 3, v243
	v_sub_u32_e32 v242, v242, v243
	v_mul_u32_u24_e32 v244, 12, v242
	v_cndmask_b32_e64 v244, v244, 20, s[66:67]
	v_add_u32_e32 v243, 2, v242
	v_mul_u32_u24_e32 v245, 11, v243
	v_lshrrev_b32_e32 v245, 5, v245
	v_mul_u32_u24_e32 v245, 3, v245
	v_sub_u32_e32 v243, v243, v245
	v_mul_u32_u24_e32 v243, 12, v243
	v_add_u32_e32 v243, -12, v243
	v_add_u32_e32 v242, 1, v242
	v_mul_u32_u24_e32 v245, 11, v242
	v_lshrrev_b32_e32 v245, 5, v245
	v_mul_u32_u24_e32 v245, 3, v245
	v_sub_u32_e32 v242, v242, v245
	v_mul_u32_u24_e32 v242, 12, v242
	v_add_u32_e32 v242, 0xffffffe8, v242
	v_cndmask_b32_e64 v242, v242, -4, s[68:69]
	v_add_u32_e32 v230, v192, v243
	v_add_u32_e32 v231, v192, v244
	v_add_u32_e32 v232, v192, v242
	v_add_u32_e32 v233, v193, v243
	v_add_u32_e32 v234, v193, v244
	v_add_u32_e32 v235, v193, v242
	v_add_u32_e32 v236, v200, v243
	v_add_u32_e32 v237, v200, v244
	v_add_u32_e32 v238, v200, v242
	v_add_u32_e32 v239, v201, v243
	v_add_u32_e32 v240, v201, v244
	v_add_u32_e32 v241, v201, v242
	s_barrier

.LBB6_159:
	s_or_b64 exec, exec, s[50:51]
	s_waitcnt lgkmcnt(3)
	v_mfma_f32_32x32x16_f16 v[26:41], v[94:97], v[50:53], v[26:41]
	ds_read_b128 v[54:57], v195 offset:13728
	ds_read_b128 v[50:53], v196 offset:13728
	s_waitcnt vmcnt(1)
	ds_write_b128 v192, v[46:49] offset:63376
	s_waitcnt vmcnt(0)
	ds_write_b32 v230, v218 offset:63908
	s_waitcnt lgkmcnt(6)
	v_mfma_f32_32x32x16_f16 v[26:41], v[86:89], v[162:165], v[26:41]
	ds_write_b32 v231, v218 offset:63896
	ds_write_b32 v232, v218 offset:63920
	s_waitcnt lgkmcnt(5)
	v_mfma_f32_32x32x16_f16 v[26:41], v[90:93], v[154:157], v[26:41]
	ds_read_b128 v[154:157], v195 offset:14784
	ds_read_b128 v[46:49], v196 offset:14784
	v_add_f32_e32 v210, v171, v22
	v_add_f32_e32 v209, v167, v23
	s_waitcnt lgkmcnt(6)
	v_mfma_f32_32x32x16_f16 v[26:41], v[82:85], v[158:161], v[26:41]
	s_and_saveexec_b64 s[50:51], s[14:15]
	s_xor_b64 s[50:51], exec, s[50:51]
	v_add_f32_e32 v209, v167, v23
	ds_write2st64_b32 v199, v210, v209 offset0:4 offset1:5
	s_andn2_saveexec_b64 s[50:51], s[50:51]
	s_or_b64 exec, exec, s[50:51]
	v_add_f32_e32 v159, v166, v24
	v_add_f32_e32 v158, v212, v25
	s_and_saveexec_b64 s[50:51], s[14:15]
	s_xor_b64 s[50:51], exec, s[50:51]
	v_add_f32_e32 v158, v212, v25
	ds_write2st64_b32 v199, v159, v158 offset0:6 offset1:7
	s_andn2_saveexec_b64 s[50:51], s[50:51]
	s_or_b64 exec, exec, s[50:51]
	s_waitcnt lgkmcnt(5)
	v_mfma_f32_32x32x16_f16 v[26:41], v[78:81], v[54:57], v[26:41]
	ds_read_b128 v[54:57], v195 offset:15840
	ds_read_b128 v[22:25], v196 offset:15840
	ds_write_b128 v193, v[42:45] offset:63376
	ds_write_b32 v233, v217 offset:63908
	s_waitcnt lgkmcnt(8)
	v_mfma_f32_32x32x16_f16 v[26:41], v[58:61], v[50:53], v[26:41]
	ds_write_b32 v234, v217 offset:63896
	ds_write_b32 v235, v217 offset:63920
	s_waitcnt lgkmcnt(5)
	v_mfma_f32_32x32x16_f16 v[26:41], v[70:73], v[154:157], v[26:41]
	s_waitcnt lgkmcnt(4)
	v_mfma_f32_32x32x16_f16 v[26:41], v[62:65], v[46:49], v[26:41]
	s_and_saveexec_b64 s[50:51], s[4:5]
	s_cbranch_execz .LBB6_176
	ds_write_b128 v200, v[6:9] offset:63376
	ds_write_b32 v236, v169 offset:63908
	ds_write_b32 v237, v169 offset:63896
	ds_write_b32 v238, v169 offset:63920
.LBB6_176:
	s_or_b64 exec, exec, s[50:51]
	s_waitcnt lgkmcnt(3)
	v_mfma_f32_32x32x16_f16 v[26:41], v[74:77], v[54:57], v[26:41]
	s_waitcnt lgkmcnt(2)
	v_mfma_f32_32x32x16_f16 v[26:41], v[66:69], v[22:25], v[26:41]
	s_and_saveexec_b64 s[50:51], s[6:7]
	s_cbranch_execz .LBB6_181
	ds_write_b128 v201, v[10:13] offset:63376
	ds_write_b32 v239, v173 offset:63908
	ds_write_b32 v240, v173 offset:63896
	ds_write_b32 v241, v173 offset:63920

.LBB6_191:
	s_or_b64 exec, exec, s[16:17]
	s_waitcnt lgkmcnt(3)
	v_mfma_f32_32x32x16_f16 v[38:53], v[94:97], v[154:157], v[38:53]
	ds_read_b128 v[158:161], v202 offset:13728
	ds_read_b128 v[154:157], v203 offset:13728
	s_waitcnt vmcnt(1)
	ds_write_b128 v192, v[54:57] offset:16
	s_waitcnt vmcnt(0)
	ds_write_b32 v230, v211 offset:548
	s_waitcnt lgkmcnt(6)
	v_mfma_f32_32x32x16_f16 v[38:53], v[86:89], v[170:173], v[38:53]
	ds_write_b32 v231, v211 offset:536
	ds_write_b32 v232, v211 offset:560
	v_add_f32_e32 v19, v3, v19
	v_add_f32_e32 v2, v2, v18
	s_waitcnt lgkmcnt(5)
	v_mfma_f32_32x32x16_f16 v[38:53], v[90:93], v[162:165], v[38:53]
	ds_read_b128 v[162:165], v202 offset:14784
	ds_read_b128 v[54:57], v203 offset:14784
	v_mov_b32_e32 v170, v34
	v_mov_b32_e32 v171, v14
	v_mov_b32_e32 v3, v30
	v_pk_add_f32 v[170:171], v[170:171], v[2:3]
	v_add_f32_e32 v209, v19, v35
	v_mov_b32_e32 v3, v27
	s_waitcnt lgkmcnt(6)
	v_mfma_f32_32x32x16_f16 v[38:53], v[82:85], v[166:169], v[38:53]
	s_and_saveexec_b64 s[16:17], s[14:15]
	s_xor_b64 s[16:17], exec, s[16:17]
	v_add_f32_e32 v209, v19, v35
	v_mov_b32_e32 v3, v27
	ds_write2st64_b32 v199, v170, v209 offset1:1
	s_andn2_saveexec_b64 s[16:17], s[16:17]
	s_or_b64 exec, exec, s[16:17]
	v_add_f32_e32 v2, v5, v21
	v_add_f32_e32 v4, v4, v20
	v_add_f32_e32 v211, v4, v36
	v_add_f32_e32 v210, v2, v37
	v_mov_b32_e32 v5, v29
	s_and_saveexec_b64 s[16:17], s[14:15]
	s_xor_b64 s[16:17], exec, s[16:17]
	v_add_f32_e32 v210, v2, v37
	v_mov_b32_e32 v5, v29
	ds_write2st64_b32 v199, v211, v210 offset0:2 offset1:3
	s_andn2_saveexec_b64 s[16:17], s[16:17]
	s_or_b64 exec, exec, s[16:17]
	s_waitcnt lgkmcnt(5)
	v_mfma_f32_32x32x16_f16 v[38:53], v[78:81], v[158:161], v[38:53]
	ds_read_b128 v[34:37], v202 offset:15840
	ds_read_b128 v[18:21], v203 offset:15840
	ds_write_b128 v193, v[22:25] offset:16
	ds_write_b32 v233, v212 offset:548
	s_waitcnt lgkmcnt(8)
	v_mfma_f32_32x32x16_f16 v[38:53], v[58:61], v[154:157], v[38:53]
	ds_write_b32 v234, v212 offset:536
	ds_write_b32 v235, v212 offset:560
	s_waitcnt lgkmcnt(5)
	v_mfma_f32_32x32x16_f16 v[38:53], v[70:73], v[162:165], v[38:53]
	s_waitcnt lgkmcnt(4)
	v_mfma_f32_32x32x16_f16 v[38:53], v[62:65], v[54:57], v[38:53]
	s_and_saveexec_b64 s[16:17], s[4:5]
	s_cbranch_execz .LBB6_208
	ds_write_b128 v200, v[10:13] offset:16
	ds_write_b32 v236, v179 offset:548
	ds_write_b32 v237, v179 offset:536
	ds_write_b32 v238, v179 offset:560
.LBB6_208:
	s_or_b64 exec, exec, s[16:17]
	s_waitcnt lgkmcnt(3)
	v_mfma_f32_32x32x16_f16 v[38:53], v[74:77], v[34:37], v[38:53]
	s_waitcnt lgkmcnt(2)
	v_mfma_f32_32x32x16_f16 v[38:53], v[66:69], v[18:21], v[38:53]
	s_and_saveexec_b64 s[16:17], s[6:7]
	s_cbranch_execz .LBB6_213
	ds_write_b128 v201, v[6:9] offset:16
	ds_write_b32 v239, v181 offset:548
	ds_write_b32 v240, v181 offset:536
	ds_write_b32 v241, v181 offset:560

.LBB6_354:
	s_or_b64 exec, exec, s[16:17]
	v_add_f32_e32 v209, v33, v9
	v_mov_b32_e32 v33, v31
	v_mov_b32_e32 v9, v7
	v_pk_add_f32 v[166:167], v[32:33], v[8:9]
	s_xor_b64 s[26:27], s[4:5], -1
	s_xor_b64 s[34:35], s[6:7], -1
	s_add_i32 s16, s3, s33
	s_bfe_u32 s17, s16, 0x30003
	s_bfe_u32 s16, s16, 0x20001
	v_lshl_or_b32 v6, s17, 2, v190
	s_lshl_b32 s40, s16, 3
	v_add_lshl_u32 v6, v6, v192, 5
	s_add_i32 s40, s40, s53
	v_add3_u32 v6, s40, v6, v193
	s_lshl_b32 s40, s59, 20
	s_lshl_b32 s17, s17, 17
	v_lshl_or_b32 v174, v6, 10, v206
	v_mov_b32_e32 v6, 0x80
	s_or_b32 s17, s40, s17
	v_lshl_or_b32 v176, v174, 2, v6
	v_lshl_or_b32 v6, v184, 15, s17
	s_lshl_b32 s16, s16, 13
	v_or_b32_e32 v6, s16, v6
	v_add_u32_e32 v7, v183, v191
	v_lshl_add_u32 v183, v7, 10, v6
	v_lshl_add_u32 v6, v169, 15, s17
	v_or_b32_e32 v6, s16, v6
	v_add_u32_e32 v7, v201, v168
	v_lshl_add_u32 v184, v7, 10, v6
	v_lshl_add_u32 v6, v173, 15, s17
	v_or_b32_e32 v6, s16, v6
	v_add_u32_e32 v7, v172, v191
	v_lshl_add_u32 v201, v7, 10, v6
	v_lshl_add_u32 v6, v200, 15, s17
	v_mov_b32_e32 v175, 0
	v_or_b32_e32 v6, s16, v6
	v_add_u32_e32 v7, v179, v178
	s_mov_b32 s54, 2
	v_mov_b32_e32 v177, v175
	v_lshl_add_u32 v200, v7, 10, v6
	v_lshlrev_b64 v[178:179], 2, v[174:175]
	s_mov_b32 s55, 0xffff7c80
	s_movk_i32 s59, 0xfc80
	s_mov_b32 s60, 0xffff7ca0
	s_movk_i32 s61, 0xfca0
	s_waitcnt lgkmcnt(0)
	v_mbcnt_lo_u32_b32 v242, -1, 0
	v_mbcnt_hi_u32_b32 v242, -1, v242
	v_and_b32_e32 v242, 31, v242
	v_cmp_eq_u32_e64 s[66:67], 0, v242
	v_cmp_eq_u32_e64 s[68:69], 31, v242
	v_mul_u32_u24_e32 v243, 11, v242
	v_lshrrev_b32_e32 v243, 5, v243
	v_mul_u32_u24_e32 v243, 3, v243
	v_sub_u32_e32 v242, v242, v243
	v_mul_u32_u24_e32 v244, 12, v242
	v_cndmask_b32_e64 v244, v244, 20, s[66:67]
	v_add_u32_e32 v243, 2, v242
	v_mul_u32_u24_e32 v245, 11, v243
	v_lshrrev_b32_e32 v245, 5, v245
	v_mul_u32_u24_e32 v245, 3, v245
	v_sub_u32_e32 v243, v243, v245
	v_mul_u32_u24_e32 v243, 12, v243
	v_add_u32_e32 v243, -12, v243
	v_add_u32_e32 v242, 1, v242
	v_mul_u32_u24_e32 v245, 11, v242
	v_lshrrev_b32_e32 v245, 5, v245
	v_mul_u32_u24_e32 v245, 3, v245
	v_sub_u32_e32 v242, v242, v245
	v_mul_u32_u24_e32 v242, 12, v242
	v_add_u32_e32 v242, 0xffffffe8, v242
	v_cndmask_b32_e64 v242, v242, -4, s[68:69]
	v_add_u32_e32 v230, v188, v243
	v_add_u32_e32 v231, v188, v244
	v_add_u32_e32 v232, v188, v242
	v_add_u32_e32 v233, v189, v243
	v_add_u32_e32 v234, v189, v244
	v_add_u32_e32 v235, v189, v242
	v_add_u32_e32 v236, v186, v243
	v_add_u32_e32 v237, v186, v244
	v_add_u32_e32 v238, v186, v242
	v_add_u32_e32 v239, v199, v243
	v_add_u32_e32 v240, v199, v244
	v_add_u32_e32 v241, v199, v242
	s_barrier

.LBB6_365:
	s_or_b64 exec, exec, s[40:41]
	s_waitcnt lgkmcnt(3)
	v_mfma_f32_32x32x16_f16 v[26:41], v[110:113], v[42:45], v[26:41]
	ds_read_b128 v[158:161], v195 offset:13728
	ds_read_b128 v[42:45], v197 offset:13728
	s_waitcnt vmcnt(1)
	ds_write_b128 v188, v[154:157] offset:63376
	s_waitcnt vmcnt(0)
	ds_write_b32 v230, v204 offset:63908
	s_waitcnt lgkmcnt(6)
	v_mfma_f32_32x32x16_f16 v[26:41], v[114:117], v[50:53], v[26:41]
	ds_write_b32 v231, v204 offset:63896
	ds_write_b32 v232, v204 offset:63920
	s_waitcnt lgkmcnt(5)
	v_mfma_f32_32x32x16_f16 v[26:41], v[118:121], v[46:49], v[26:41]
	ds_read_b128 v[50:53], v195 offset:14784
	ds_read_b128 v[46:49], v197 offset:14784
	v_add_f32_e32 v205, v171, v22
	v_add_f32_e32 v207, v167, v23
	s_waitcnt lgkmcnt(6)
	v_mfma_f32_32x32x16_f16 v[26:41], v[122:125], v[162:165], v[26:41]
	s_and_saveexec_b64 s[40:41], s[14:15]
	s_xor_b64 s[40:41], exec, s[40:41]
	v_add_f32_e32 v207, v167, v23
	ds_write2st64_b32 v185, v205, v207 offset0:4 offset1:5
	s_andn2_saveexec_b64 s[40:41], s[40:41]
	s_or_b64 exec, exec, s[40:41]
	v_add_f32_e32 v210, v166, v24
	v_add_f32_e32 v208, v209, v25
	s_and_saveexec_b64 s[40:41], s[14:15]
	s_xor_b64 s[40:41], exec, s[40:41]
	v_add_f32_e32 v208, v209, v25
	ds_write2st64_b32 v185, v210, v208 offset0:6 offset1:7
	s_andn2_saveexec_b64 s[40:41], s[40:41]
	s_or_b64 exec, exec, s[40:41]
	s_waitcnt lgkmcnt(5)
	v_mfma_f32_32x32x16_f16 v[26:41], v[126:129], v[158:161], v[26:41]
	ds_read_b128 v[158:161], v195 offset:15840
	ds_read_b128 v[22:25], v197 offset:15840
	ds_write_b128 v189, v[6:9] offset:63376
	ds_write_b32 v233, v202 offset:63908
	s_waitcnt lgkmcnt(8)
	v_mfma_f32_32x32x16_f16 v[26:41], v[130:133], v[42:45], v[26:41]
	ds_write_b32 v234, v202 offset:63896
	ds_write_b32 v235, v202 offset:63920
	s_waitcnt lgkmcnt(5)
	v_mfma_f32_32x32x16_f16 v[26:41], v[134:137], v[50:53], v[26:41]
	s_waitcnt lgkmcnt(4)
	v_mfma_f32_32x32x16_f16 v[26:41], v[138:141], v[46:49], v[26:41]
	s_and_saveexec_b64 s[40:41], s[4:5]
	s_cbranch_execz .LBB6_382
	ds_write_b128 v186, v[150:153] offset:63376
	ds_write_b32 v236, v203 offset:63908
	ds_write_b32 v237, v203 offset:63896
	ds_write_b32 v238, v203 offset:63920
.LBB6_382:
	s_or_b64 exec, exec, s[40:41]
	s_waitcnt lgkmcnt(3)
	v_mfma_f32_32x32x16_f16 v[26:41], v[142:145], v[158:161], v[26:41]
	s_waitcnt lgkmcnt(2)
	v_mfma_f32_32x32x16_f16 v[26:41], v[146:149], v[22:25], v[26:41]
	s_and_saveexec_b64 s[40:41], s[6:7]
	s_cbranch_execz .LBB6_387
	ds_write_b128 v199, v[10:13] offset:63376
	ds_write_b32 v239, v174 offset:63908
	ds_write_b32 v240, v174 offset:63896
	ds_write_b32 v241, v174 offset:63920

.LBB6_399:
	s_or_b64 exec, exec, s[16:17]
	s_waitcnt lgkmcnt(3)
	v_mfma_f32_32x32x16_f16 v[38:53], v[110:113], v[22:25], v[38:53]
	ds_read_b128 v[158:161], v196 offset:13728
	ds_read_b128 v[22:25], v198 offset:13728
	v_cndmask_b32_e64 v205, 0, 1, s[48:49]
	v_cmp_ne_u32_e64 s[16:17], 1, v205
	s_andn2_b64 vcc, exec, s[48:49]
	s_waitcnt lgkmcnt(4)
	v_mfma_f32_32x32x16_f16 v[38:53], v[114:117], v[170:173], v[38:53]
	s_cbranch_vccnz .LBB6_405
	s_waitcnt vmcnt(1)
	ds_write_b128 v188, v[154:157] offset:16
	s_waitcnt vmcnt(0)
	ds_write_b32 v230, v204 offset:548
	ds_write_b32 v231, v204 offset:536
	ds_write_b32 v232, v204 offset:560
.LBB6_405:
	v_add_f32_e32 v19, v3, v19
	v_add_f32_e32 v2, v2, v18
	s_waitcnt lgkmcnt(3)
	v_mfma_f32_32x32x16_f16 v[38:53], v[118:121], v[162:165], v[38:53]
	ds_read_b128 v[162:165], v196 offset:14784
	s_waitcnt vmcnt(1)
	ds_read_b128 v[154:157], v198 offset:14784
	v_mov_b32_e32 v170, v34
	v_mov_b32_e32 v171, v14
	v_mov_b32_e32 v3, v30
	v_pk_add_f32 v[170:171], v[170:171], v[2:3]
	v_add_f32_e32 v205, v19, v35
	v_mov_b32_e32 v3, v27
	s_waitcnt lgkmcnt(4)
	v_mfma_f32_32x32x16_f16 v[38:53], v[122:125], v[166:169], v[38:53]
	s_and_saveexec_b64 s[42:43], s[14:15]
	s_xor_b64 s[42:43], exec, s[42:43]
	v_add_f32_e32 v205, v19, v35
	v_mov_b32_e32 v3, v27
	ds_write2st64_b32 v185, v170, v205 offset1:1
	s_andn2_saveexec_b64 s[42:43], s[42:43]
	s_or_b64 exec, exec, s[42:43]
	v_add_f32_e32 v2, v5, v21
	v_add_f32_e32 v4, v4, v20
	v_add_f32_e32 v208, v4, v36
	v_add_f32_e32 v207, v2, v37
	v_mov_b32_e32 v5, v29
	s_and_saveexec_b64 s[42:43], s[14:15]
	s_xor_b64 s[42:43], exec, s[42:43]
	v_add_f32_e32 v207, v2, v37
	v_mov_b32_e32 v5, v29
	ds_write2st64_b32 v185, v208, v207 offset0:2 offset1:3
	s_andn2_saveexec_b64 s[42:43], s[42:43]
	s_or_b64 exec, exec, s[42:43]
	s_waitcnt lgkmcnt(3)
	v_mfma_f32_32x32x16_f16 v[38:53], v[126:129], v[158:161], v[38:53]
	ds_read_b128 v[34:37], v196 offset:15840
	ds_read_b128 v[18:21], v198 offset:15840
	s_and_b64 vcc, exec, s[16:17]
	s_waitcnt lgkmcnt(4)
	v_mfma_f32_32x32x16_f16 v[38:53], v[130:133], v[22:25], v[38:53]
	s_cbranch_vccnz .LBB6_415
	ds_write_b128 v189, v[6:9] offset:16
	s_waitcnt vmcnt(0)
	ds_write_b32 v233, v202 offset:548
	ds_write_b32 v234, v202 offset:536
	ds_write_b32 v235, v202 offset:560
.LBB6_415:
	s_waitcnt lgkmcnt(3)
	v_mfma_f32_32x32x16_f16 v[38:53], v[134:137], v[162:165], v[38:53]
	s_nor_b64 s[42:43], s[40:41], s[26:27]
	s_waitcnt lgkmcnt(2)
	v_mfma_f32_32x32x16_f16 v[38:53], v[138:141], v[154:157], v[38:53]
	s_and_saveexec_b64 s[16:17], s[42:43]
	s_cbranch_execz .LBB6_420
	ds_write_b128 v186, v[150:153] offset:16
	s_waitcnt vmcnt(0)
	ds_write_b32 v236, v203 offset:548
	ds_write_b32 v237, v203 offset:536
	ds_write_b32 v238, v203 offset:560
.LBB6_420:
	s_or_b64 exec, exec, s[16:17]
	s_waitcnt lgkmcnt(1)
	v_mfma_f32_32x32x16_f16 v[38:53], v[142:145], v[34:37], v[38:53]
	s_nor_b64 s[40:41], s[40:41], s[34:35]
	s_waitcnt lgkmcnt(0)
	v_mfma_f32_32x32x16_f16 v[38:53], v[146:149], v[18:21], v[38:53]
	s_and_saveexec_b64 s[16:17], s[40:41]
	s_cbranch_execz .LBB6_425
	ds_write_b128 v199, v[10:13] offset:16
	s_waitcnt vmcnt(0)
	ds_write_b32 v239, v174 offset:548
	ds_write_b32 v240, v174 offset:536
	ds_write_b32 v241, v174 offset:560

	.amdhsa_kernel _Z8k23_mfmaPK15HIP_vector_typeIjLj4EEPKjS2_PKfPS0_PjS2_S4_S2_S6_Pf
		.amdhsa_group_segment_fixed_size 0
		.amdhsa_private_segment_fixed_size 0
		.amdhsa_kernarg_size 88
		.amdhsa_user_sgpr_count 2
		.amdhsa_user_sgpr_dispatch_ptr 0
		.amdhsa_user_sgpr_queue_ptr 0
		.amdhsa_user_sgpr_kernarg_segment_ptr 1
		.amdhsa_user_sgpr_dispatch_id 0
		.amdhsa_user_sgpr_kernarg_preload_length 0
		.amdhsa_user_sgpr_kernarg_preload_offset 0
		.amdhsa_user_sgpr_private_segment_size 0
		.amdhsa_uses_dynamic_stack 0
		.amdhsa_enable_private_segment 0
		.amdhsa_system_sgpr_workgroup_id_x 1
		.amdhsa_system_sgpr_workgroup_id_y 0
		.amdhsa_system_sgpr_workgroup_id_z 0
		.amdhsa_system_sgpr_workgroup_info 0
		.amdhsa_system_vgpr_workitem_id 0
		.amdhsa_next_free_vgpr 256
		.amdhsa_next_free_sgpr 70
		.amdhsa_accum_offset 256
		.amdhsa_reserve_vcc 1
		.amdhsa_float_round_mode_32 0
		.amdhsa_float_round_mode_16_64 0
		.amdhsa_float_denorm_mode_32 3
		.amdhsa_float_denorm_mode_16_64 3
		.amdhsa_dx10_clamp 1
		.amdhsa_ieee_mode 1
		.amdhsa_fp16_overflow 0
		.amdhsa_tg_split 0
		.amdhsa_exception_fp_ieee_invalid_op 0
		.amdhsa_exception_fp_denorm_src 0
		.amdhsa_exception_fp_ieee_div_zero 0
		.amdhsa_exception_fp_ieee_overflow 0
		.amdhsa_exception_fp_ieee_underflow 0
		.amdhsa_exception_fp_ieee_inexact 0
		.amdhsa_exception_int_div_zero 0
	.end_amdhsa_kernel

.LBB8_145:
	s_or_b64 exec, exec, s[14:15]
	v_add_f32_e32 v224, v45, v9
	v_mov_b32_e32 v45, v43
	v_mov_b32_e32 v9, v7
	v_pk_add_f32 v[166:167], v[44:45], v[8:9]
	v_add_u32_e32 v6, s33, v191
	v_add_lshl_u32 v6, v6, v208, 5
	s_add_i32 s14, s50, s56
	v_add3_u32 v6, s14, v6, v207
	s_lshl_b32 s15, s52, 15
	v_lshl_or_b32 v6, v6, 10, v190
	s_lshl_b32 s14, s53, 20
	s_and_b32 s15, s15, 0xe0000
	v_ashrrev_i32_e32 v7, 31, v6
	s_or_b32 s14, s14, s15
	s_lshl_b32 s15, s51, 12
	v_lshl_add_u64 v[174:175], v[6:7], 2, s[24:25]
	v_lshl_add_u32 v6, v182, 15, s14
	s_and_b32 s15, s15, 0x6000
	v_or_b32_e32 v6, s15, v6
	v_add_u32_e32 v7, v177, v176
	v_lshl_add_u32 v217, v7, 10, v6
	v_or_b32_e32 v6, v217, v190
	v_add_u32_e32 v6, 0xffff7c00, v6
	v_ashrrev_i32_e32 v7, 31, v6
	v_lshl_add_u64 v[176:177], v[6:7], 2, s[18:19]
	v_lshl_add_u32 v6, v179, 15, s14
	v_or_b32_e32 v6, s15, v6
	v_add_u32_e32 v7, v178, v193
	v_lshl_add_u32 v218, v7, 10, v6
	v_or_b32_e32 v6, v218, v190
	v_add_u32_e32 v6, 0xfffffc00, v6
	v_ashrrev_i32_e32 v7, 31, v6
	v_lshl_add_u64 v[178:179], v[6:7], 2, s[18:19]
	v_lshl_add_u32 v6, v181, 15, s14
	v_or_b32_e32 v6, s15, v6
	v_add_u32_e32 v7, v183, v180
	v_lshl_add_u32 v219, v7, 10, v6
	v_or_b32_e32 v6, v219, v190
	v_add_u32_e32 v6, 0xffff7c00, v6
	v_ashrrev_i32_e32 v7, 31, v6
	v_lshl_add_u64 v[180:181], v[6:7], 2, s[18:19]
	v_lshl_or_b32 v6, v195, 15, s14
	v_or_b32_e32 v6, s15, v6
	v_add_u32_e32 v7, v194, v193
	v_lshl_add_u32 v220, v7, 10, v6
	v_or_b32_e32 v6, v220, v190
	v_add_u32_e32 v6, 0xffff7c00, v6
	v_ashrrev_i32_e32 v7, 31, v6
	s_mov_b32 s57, 2
	v_lshl_add_u64 v[182:183], v[6:7], 2, s[18:19]
	v_mov_b32_e32 v213, 0
	s_mov_b64 s[36:37], 0
	s_mov_b32 s58, 0xffff7e80
	s_movk_i32 s59, 0xfe80
	s_mov_b32 s60, 0xffff7ea0
	s_movk_i32 s61, 0xfea0
	v_mov_b32_e32 v216, 0
	v_mov_b32_e32 v215, 0
	v_mov_b32_e32 v214, 0
	s_waitcnt lgkmcnt(0)
	v_mbcnt_lo_u32_b32 v250, -1, 0
	v_mbcnt_hi_u32_b32 v250, -1, v250
	v_and_b32_e32 v250, 31, v250
	v_cmp_eq_u32_e64 s[64:65], 0, v250
	v_cmp_eq_u32_e64 s[66:67], 31, v250
	v_mul_u32_u24_e32 v251, 11, v250
	v_lshrrev_b32_e32 v251, 5, v251
	v_mul_u32_u24_e32 v251, 3, v251
	v_sub_u32_e32 v250, v250, v251
	v_mul_u32_u24_e32 v252, 12, v250
	v_cndmask_b32_e64 v252, v252, 20, s[64:65]
	v_add_u32_e32 v251, 2, v250
	v_mul_u32_u24_e32 v253, 11, v251
	v_lshrrev_b32_e32 v253, 5, v253
	v_mul_u32_u24_e32 v253, 3, v253
	v_sub_u32_e32 v251, v251, v253
	v_mul_u32_u24_e32 v251, 12, v251
	v_add_u32_e32 v251, -12, v251
	v_add_u32_e32 v250, 1, v250
	v_mul_u32_u24_e32 v253, 11, v250
	v_lshrrev_b32_e32 v253, 5, v253
	v_mul_u32_u24_e32 v253, 3, v253
	v_sub_u32_e32 v250, v250, v253
	v_mul_u32_u24_e32 v250, 12, v250
	v_add_u32_e32 v250, 0xffffffe8, v250
	v_cndmask_b32_e64 v250, v250, -4, s[66:67]
	v_add_u32_e32 v238, v202, v251
	v_add_u32_e32 v239, v202, v252
	v_add_u32_e32 v240, v202, v250
	v_add_u32_e32 v241, v203, v251
	v_add_u32_e32 v242, v203, v252
	v_add_u32_e32 v243, v203, v250
	v_add_u32_e32 v244, v209, v251
	v_add_u32_e32 v245, v209, v252
	v_add_u32_e32 v246, v209, v250
	v_add_u32_e32 v247, v210, v251
	v_add_u32_e32 v248, v210, v252
	v_add_u32_e32 v249, v210, v250
	s_barrier

.LBB8_158:
	s_or_b64 exec, exec, s[44:45]
	s_waitcnt lgkmcnt(3)
	v_mfma_f32_32x32x16_f16 v[26:41], v[94:97], v[50:53], v[26:41]
	ds_read_b128 v[54:57], v204 offset:13728
	ds_read_b128 v[50:53], v205 offset:13728
	s_waitcnt vmcnt(1)
	ds_write_b128 v202, v[46:49] offset:63376
	s_waitcnt vmcnt(0)
	ds_write_b32 v238, v226 offset:63908
	s_waitcnt lgkmcnt(6)
	v_mfma_f32_32x32x16_f16 v[26:41], v[86:89], v[162:165], v[26:41]
	ds_write_b32 v239, v226 offset:63896
	ds_write_b32 v240, v226 offset:63920
	s_waitcnt lgkmcnt(5)
	v_mfma_f32_32x32x16_f16 v[26:41], v[90:93], v[154:157], v[26:41]
	ds_read_b128 v[154:157], v204 offset:14784
	ds_read_b128 v[46:49], v205 offset:14784
	v_add_f32_e32 v221, v171, v22
	v_add_f32_e32 v222, v167, v23
	s_waitcnt lgkmcnt(6)
	v_mfma_f32_32x32x16_f16 v[26:41], v[82:85], v[158:161], v[26:41]
	s_and_saveexec_b64 s[44:45], s[12:13]
	s_xor_b64 s[44:45], exec, s[44:45]
	v_add_f32_e32 v222, v167, v23
	ds_write2st64_b32 v206, v221, v222 offset0:4 offset1:5
	s_andn2_saveexec_b64 s[44:45], s[44:45]
	s_or_b64 exec, exec, s[44:45]
	v_add_f32_e32 v226, v166, v24
	v_add_f32_e32 v223, v224, v25
	s_and_saveexec_b64 s[44:45], s[12:13]
	s_xor_b64 s[44:45], exec, s[44:45]
	v_add_f32_e32 v223, v224, v25
	ds_write2st64_b32 v206, v226, v223 offset0:6 offset1:7
	s_andn2_saveexec_b64 s[44:45], s[44:45]
	s_or_b64 exec, exec, s[44:45]
	s_waitcnt lgkmcnt(5)
	v_mfma_f32_32x32x16_f16 v[26:41], v[78:81], v[54:57], v[26:41]
	ds_read_b128 v[54:57], v204 offset:15840
	ds_read_b128 v[22:25], v205 offset:15840
	ds_write_b128 v203, v[42:45] offset:63376
	ds_write_b32 v241, v228 offset:63908
	s_waitcnt lgkmcnt(8)
	v_mfma_f32_32x32x16_f16 v[26:41], v[58:61], v[50:53], v[26:41]
	ds_write_b32 v242, v228 offset:63896
	ds_write_b32 v243, v228 offset:63920
	s_waitcnt lgkmcnt(5)
	v_mfma_f32_32x32x16_f16 v[26:41], v[70:73], v[154:157], v[26:41]
	s_waitcnt lgkmcnt(4)
	v_mfma_f32_32x32x16_f16 v[26:41], v[62:65], v[46:49], v[26:41]
	s_and_saveexec_b64 s[44:45], s[2:3]
	s_cbranch_execz .LBB8_175
	ds_write_b128 v209, v[10:13] offset:63376
	ds_write_b32 v244, v225 offset:63908
	ds_write_b32 v245, v225 offset:63896
	ds_write_b32 v246, v225 offset:63920
.LBB8_175:
	s_or_b64 exec, exec, s[44:45]
	s_waitcnt lgkmcnt(3)
	v_mfma_f32_32x32x16_f16 v[26:41], v[74:77], v[54:57], v[26:41]
	s_waitcnt lgkmcnt(2)
	v_mfma_f32_32x32x16_f16 v[26:41], v[66:69], v[22:25], v[26:41]
	s_and_saveexec_b64 s[44:45], s[4:5]
	s_cbranch_execz .LBB8_180
	ds_write_b128 v210, v[6:9] offset:63376
	ds_write_b32 v247, v227 offset:63908
	ds_write_b32 v248, v227 offset:63896
	ds_write_b32 v249, v227 offset:63920

.LBB8_192:
	s_or_b64 exec, exec, s[14:15]
	s_waitcnt lgkmcnt(3)
	v_mfma_f32_32x32x16_f16 v[38:53], v[94:97], v[154:157], v[38:53]
	ds_read_b128 v[158:161], v211 offset:13728
	ds_read_b128 v[154:157], v212 offset:13728
	s_waitcnt vmcnt(1)
	ds_write_b128 v202, v[54:57] offset:16
	s_waitcnt vmcnt(0)
	ds_write_b32 v238, v228 offset:548
	s_waitcnt lgkmcnt(6)
	v_mfma_f32_32x32x16_f16 v[38:53], v[86:89], v[170:173], v[38:53]
	ds_write_b32 v239, v228 offset:536
	ds_write_b32 v240, v228 offset:560
	v_add_f32_e32 v19, v3, v19
	v_add_f32_e32 v2, v2, v18
	s_waitcnt lgkmcnt(5)
	v_mfma_f32_32x32x16_f16 v[38:53], v[90:93], v[162:165], v[38:53]
	ds_read_b128 v[162:165], v211 offset:14784
	ds_read_b128 v[54:57], v212 offset:14784
	v_mov_b32_e32 v170, v34
	v_mov_b32_e32 v171, v14
	v_mov_b32_e32 v3, v30
	v_pk_add_f32 v[170:171], v[170:171], v[2:3]
	v_add_f32_e32 v221, v19, v35
	v_mov_b32_e32 v3, v27
	s_waitcnt lgkmcnt(6)
	v_mfma_f32_32x32x16_f16 v[38:53], v[82:85], v[166:169], v[38:53]
	s_and_saveexec_b64 s[14:15], s[12:13]
	s_xor_b64 s[14:15], exec, s[14:15]
	v_add_f32_e32 v221, v19, v35
	v_mov_b32_e32 v3, v27
	ds_write2st64_b32 v206, v170, v221 offset1:1
	s_andn2_saveexec_b64 s[14:15], s[14:15]
	s_or_b64 exec, exec, s[14:15]
	v_add_f32_e32 v2, v5, v21
	v_add_f32_e32 v4, v4, v20
	v_add_f32_e32 v223, v4, v36
	v_add_f32_e32 v222, v2, v37
	v_mov_b32_e32 v5, v29
	s_and_saveexec_b64 s[14:15], s[12:13]
	s_xor_b64 s[14:15], exec, s[14:15]
	v_add_f32_e32 v222, v2, v37
	v_mov_b32_e32 v5, v29
	ds_write2st64_b32 v206, v223, v222 offset0:2 offset1:3
	s_andn2_saveexec_b64 s[14:15], s[14:15]
	s_or_b64 exec, exec, s[14:15]
	s_waitcnt lgkmcnt(5)
	v_mfma_f32_32x32x16_f16 v[38:53], v[78:81], v[158:161], v[38:53]
	ds_read_b128 v[34:37], v211 offset:15840
	ds_read_b128 v[18:21], v212 offset:15840
	ds_write_b128 v203, v[22:25] offset:16
	ds_write_b32 v241, v225 offset:548
	s_waitcnt lgkmcnt(8)
	v_mfma_f32_32x32x16_f16 v[38:53], v[58:61], v[154:157], v[38:53]
	ds_write_b32 v242, v225 offset:536
	ds_write_b32 v243, v225 offset:560
	s_waitcnt lgkmcnt(5)
	v_mfma_f32_32x32x16_f16 v[38:53], v[70:73], v[162:165], v[38:53]
	s_waitcnt lgkmcnt(4)
	v_mfma_f32_32x32x16_f16 v[38:53], v[62:65], v[54:57], v[38:53]
	s_and_saveexec_b64 s[14:15], s[2:3]
	s_cbranch_execz .LBB8_209
	ds_write_b128 v209, v[10:13] offset:16
	ds_write_b32 v244, v227 offset:548
	ds_write_b32 v245, v227 offset:536
	ds_write_b32 v246, v227 offset:560
.LBB8_209:
	s_or_b64 exec, exec, s[14:15]
	s_waitcnt lgkmcnt(3)
	v_mfma_f32_32x32x16_f16 v[38:53], v[74:77], v[34:37], v[38:53]
	s_waitcnt lgkmcnt(2)
	v_mfma_f32_32x32x16_f16 v[38:53], v[66:69], v[18:21], v[38:53]
	s_and_saveexec_b64 s[14:15], s[4:5]
	s_cbranch_execz .LBB8_214
	ds_write_b128 v210, v[6:9] offset:16
	ds_write_b32 v247, v224 offset:548
	ds_write_b32 v248, v224 offset:536
	ds_write_b32 v249, v224 offset:560

.LBB8_357:
	s_or_b64 exec, exec, s[14:15]
	v_add_f32_e32 v179, v31, v7
	v_mov_b32_e32 v31, v29
	v_mov_b32_e32 v7, v5
	v_pk_add_f32 v[166:167], v[30:31], v[6:7]
	s_xor_b64 s[22:23], s[2:3], -1
	s_xor_b64 s[26:27], s[4:5], -1
	v_add3_u32 v4, v191, s33, v185
	s_add_i32 s14, s50, s47
	v_lshl_add_u32 v4, v4, 5, s14
	s_lshl_b32 s15, s53, 20
	s_lshl_b32 s34, s51, 12
	v_add_lshl_u32 v199, v4, v186, 10
	v_lshl_or_b32 v4, v195, 15, s15
	s_and_b32 s34, s34, 0x6000
	v_or_b32_e32 v4, s34, v4
	v_add_u32_e32 v5, v194, v193
	v_lshl_add_u32 v194, v5, 10, v4
	v_lshl_add_u32 v4, v165, 15, s15
	v_or_b32_e32 v4, s34, v4
	v_add_u32_e32 v5, v175, v164
	v_lshl_add_u32 v201, v5, 10, v4
	v_lshl_or_b32 v4, v171, 15, s15
	v_or_b32_e32 v4, s34, v4
	v_add_u32_e32 v5, v170, v193
	s_lshl_b32 s14, s52, 15
	v_lshl_add_u32 v193, v5, 10, v4
	v_lshl_add_u32 v4, v174, 15, s15
	s_and_b32 s14, s14, 0xe0000
	v_or_b32_e32 v4, s34, v4
	v_add_u32_e32 v5, v173, v172
	v_or_b32_e32 v195, s14, v190
	v_lshl_add_u32 v202, v5, 10, v4
	v_mov_b32_e32 v203, 0
	s_mov_b32 s48, 2
	s_mov_b32 s49, 0xffff7c80
	s_movk_i32 s51, 0xfc80
	s_mov_b32 s52, 0xffff7ca0
	s_movk_i32 s53, 0xfca0
	v_mov_b32_e32 v204, 0
	v_mov_b32_e32 v205, 0
	v_mov_b32_e32 v206, 0
	s_waitcnt lgkmcnt(0)
	v_mbcnt_lo_u32_b32 v250, -1, 0
	v_mbcnt_hi_u32_b32 v250, -1, v250
	v_and_b32_e32 v250, 31, v250
	v_cmp_eq_u32_e64 s[64:65], 0, v250
	v_cmp_eq_u32_e64 s[66:67], 31, v250
	v_mul_u32_u24_e32 v251, 11, v250
	v_lshrrev_b32_e32 v251, 5, v251
	v_mul_u32_u24_e32 v251, 3, v251
	v_sub_u32_e32 v250, v250, v251
	v_mul_u32_u24_e32 v252, 12, v250
	v_cndmask_b32_e64 v252, v252, 20, s[64:65]
	v_add_u32_e32 v251, 2, v250
	v_mul_u32_u24_e32 v253, 11, v251
	v_lshrrev_b32_e32 v253, 5, v253
	v_mul_u32_u24_e32 v253, 3, v253
	v_sub_u32_e32 v251, v251, v253
	v_mul_u32_u24_e32 v251, 12, v251
	v_add_u32_e32 v251, -12, v251
	v_add_u32_e32 v250, 1, v250
	v_mul_u32_u24_e32 v253, 11, v250
	v_lshrrev_b32_e32 v253, 5, v253
	v_mul_u32_u24_e32 v253, 3, v253
	v_sub_u32_e32 v250, v250, v253
	v_mul_u32_u24_e32 v250, 12, v250
	v_add_u32_e32 v250, 0xffffffe8, v250
	v_cndmask_b32_e64 v250, v250, -4, s[66:67]
	v_add_u32_e32 v238, v183, v251
	v_add_u32_e32 v239, v183, v252
	v_add_u32_e32 v240, v183, v250
	v_add_u32_e32 v241, v184, v251
	v_add_u32_e32 v242, v184, v252
	v_add_u32_e32 v243, v184, v250
	v_add_u32_e32 v244, v197, v251
	v_add_u32_e32 v245, v197, v252
	v_add_u32_e32 v246, v197, v250
	v_add_u32_e32 v247, v198, v251
	v_add_u32_e32 v248, v198, v252
	v_add_u32_e32 v249, v198, v250
	s_barrier

.LBB8_370:
	s_or_b64 exec, exec, s[34:35]
	s_waitcnt lgkmcnt(3)
	v_mfma_f32_32x32x16_f16 v[24:39], v[108:111], v[40:43], v[24:39]
	ds_read_b128 v[156:159], v187 offset:13728
	ds_read_b128 v[40:43], v189 offset:13728
	s_waitcnt vmcnt(1)
	ds_write_b128 v183, v[152:155] offset:63376
	s_waitcnt vmcnt(0)
	ds_write_b32 v238, v210 offset:63908
	s_waitcnt lgkmcnt(6)
	v_mfma_f32_32x32x16_f16 v[24:39], v[112:115], v[48:51], v[24:39]
	ds_write_b32 v239, v210 offset:63896
	ds_write_b32 v240, v210 offset:63920
	s_waitcnt lgkmcnt(5)
	v_mfma_f32_32x32x16_f16 v[24:39], v[116:119], v[44:47], v[24:39]
	ds_read_b128 v[48:51], v187 offset:14784
	ds_read_b128 v[44:47], v189 offset:14784
	v_add_f32_e32 v211, v169, v20
	v_add_f32_e32 v212, v167, v21
	s_waitcnt lgkmcnt(6)
	v_mfma_f32_32x32x16_f16 v[24:39], v[120:123], v[160:163], v[24:39]
	s_and_saveexec_b64 s[34:35], s[12:13]
	s_xor_b64 s[34:35], exec, s[34:35]
	v_add_f32_e32 v212, v167, v21
	ds_write2st64_b32 v196, v211, v212 offset0:4 offset1:5
	s_andn2_saveexec_b64 s[34:35], s[34:35]
	s_or_b64 exec, exec, s[34:35]
	v_add_f32_e32 v214, v166, v22
	v_add_f32_e32 v213, v179, v23
	s_and_saveexec_b64 s[34:35], s[12:13]
	s_xor_b64 s[34:35], exec, s[34:35]
	v_add_f32_e32 v213, v179, v23
	ds_write2st64_b32 v196, v214, v213 offset0:6 offset1:7
	s_andn2_saveexec_b64 s[34:35], s[34:35]
	s_or_b64 exec, exec, s[34:35]
	s_waitcnt lgkmcnt(5)
	v_mfma_f32_32x32x16_f16 v[24:39], v[124:127], v[156:159], v[24:39]
	ds_read_b128 v[156:159], v187 offset:15840
	ds_read_b128 v[20:23], v189 offset:15840
	ds_write_b128 v184, v[4:7] offset:63376
	ds_write_b32 v241, v207 offset:63908
	s_waitcnt lgkmcnt(8)
	v_mfma_f32_32x32x16_f16 v[24:39], v[128:131], v[40:43], v[24:39]
	ds_write_b32 v242, v207 offset:63896
	ds_write_b32 v243, v207 offset:63920
	s_waitcnt lgkmcnt(5)
	v_mfma_f32_32x32x16_f16 v[24:39], v[132:135], v[48:51], v[24:39]
	s_waitcnt lgkmcnt(4)
	v_mfma_f32_32x32x16_f16 v[24:39], v[136:139], v[44:47], v[24:39]
	s_and_saveexec_b64 s[34:35], s[2:3]
	s_cbranch_execz .LBB8_387
	ds_write_b128 v197, v[148:151] offset:63376
	ds_write_b32 v244, v208 offset:63908
	ds_write_b32 v245, v208 offset:63896
	ds_write_b32 v246, v208 offset:63920
.LBB8_387:
	s_or_b64 exec, exec, s[34:35]
	s_waitcnt lgkmcnt(3)
	v_mfma_f32_32x32x16_f16 v[24:39], v[140:143], v[156:159], v[24:39]
	s_waitcnt lgkmcnt(2)
	v_mfma_f32_32x32x16_f16 v[24:39], v[144:147], v[20:23], v[24:39]
	s_and_saveexec_b64 s[34:35], s[4:5]
	s_cbranch_execz .LBB8_392
	ds_write_b128 v198, v[8:11] offset:63376
	ds_write_b32 v247, v209 offset:63908
	ds_write_b32 v248, v209 offset:63896
	ds_write_b32 v249, v209 offset:63920

.LBB8_406:
	s_or_b64 exec, exec, s[14:15]
	s_waitcnt lgkmcnt(3)
	v_mfma_f32_32x32x16_f16 v[36:51], v[108:111], v[20:23], v[36:51]
	ds_read_b128 v[156:159], v188 offset:13728
	ds_read_b128 v[20:23], v200 offset:13728
	v_cndmask_b32_e64 v172, 0, 1, s[42:43]
	v_cmp_ne_u32_e64 s[14:15], 1, v172
	s_andn2_b64 vcc, exec, s[42:43]
	s_waitcnt lgkmcnt(4)
	v_mfma_f32_32x32x16_f16 v[36:51], v[112:115], v[168:171], v[36:51]
	s_cbranch_vccnz .LBB8_412
	s_waitcnt vmcnt(1)
	ds_write_b128 v183, v[152:155] offset:16
	s_waitcnt vmcnt(0)
	ds_write_b32 v238, v210 offset:548
	ds_write_b32 v239, v210 offset:536
	ds_write_b32 v240, v210 offset:560
.LBB8_412:
	v_add_f32_e32 v17, v1, v17
	v_add_f32_e32 v0, v0, v16
	s_waitcnt lgkmcnt(3)
	v_mfma_f32_32x32x16_f16 v[36:51], v[116:119], v[160:163], v[36:51]
	ds_read_b128 v[160:163], v188 offset:14784
	s_waitcnt vmcnt(1)
	ds_read_b128 v[152:155], v200 offset:14784
	v_mov_b32_e32 v168, v32
	v_mov_b32_e32 v169, v12
	v_mov_b32_e32 v1, v28
	v_pk_add_f32 v[168:169], v[168:169], v[0:1]
	v_add_f32_e32 v176, v17, v33
	v_mov_b32_e32 v1, v25
	s_waitcnt lgkmcnt(4)
	v_mfma_f32_32x32x16_f16 v[36:51], v[120:123], v[164:167], v[36:51]
	s_and_saveexec_b64 s[36:37], s[12:13]
	s_xor_b64 s[36:37], exec, s[36:37]
	v_add_f32_e32 v176, v17, v33
	v_mov_b32_e32 v1, v25
	ds_write2st64_b32 v196, v168, v176 offset1:1
	s_andn2_saveexec_b64 s[36:37], s[36:37]
	s_or_b64 exec, exec, s[36:37]
	v_add_f32_e32 v0, v3, v19
	v_add_f32_e32 v2, v2, v18
	v_add_f32_e32 v178, v2, v34
	v_add_f32_e32 v177, v0, v35
	v_mov_b32_e32 v3, v27
	s_and_saveexec_b64 s[36:37], s[12:13]
	s_xor_b64 s[36:37], exec, s[36:37]
	v_add_f32_e32 v177, v0, v35
	v_mov_b32_e32 v3, v27
	ds_write2st64_b32 v196, v178, v177 offset0:2 offset1:3
	s_andn2_saveexec_b64 s[36:37], s[36:37]
	s_or_b64 exec, exec, s[36:37]
	s_waitcnt lgkmcnt(3)
	v_mfma_f32_32x32x16_f16 v[36:51], v[124:127], v[156:159], v[36:51]
	ds_read_b128 v[32:35], v188 offset:15840
	ds_read_b128 v[16:19], v200 offset:15840
	s_and_b64 vcc, exec, s[14:15]
	s_waitcnt lgkmcnt(4)
	v_mfma_f32_32x32x16_f16 v[36:51], v[128:131], v[20:23], v[36:51]
	s_cbranch_vccnz .LBB8_422
	ds_write_b128 v184, v[4:7] offset:16
	s_waitcnt vmcnt(0)
	ds_write_b32 v241, v207 offset:548
	ds_write_b32 v242, v207 offset:536
	ds_write_b32 v243, v207 offset:560
.LBB8_422:
	s_waitcnt lgkmcnt(3)
	v_mfma_f32_32x32x16_f16 v[36:51], v[132:135], v[160:163], v[36:51]
	s_nor_b64 s[36:37], s[34:35], s[22:23]
	s_waitcnt lgkmcnt(2)
	v_mfma_f32_32x32x16_f16 v[36:51], v[136:139], v[152:155], v[36:51]
	s_and_saveexec_b64 s[14:15], s[36:37]
	s_cbranch_execz .LBB8_427
	ds_write_b128 v197, v[148:151] offset:16
	s_waitcnt vmcnt(0)
	ds_write_b32 v244, v208 offset:548
	ds_write_b32 v245, v208 offset:536
	ds_write_b32 v246, v208 offset:560
.LBB8_427:
	s_or_b64 exec, exec, s[14:15]
	s_waitcnt lgkmcnt(1)
	v_mfma_f32_32x32x16_f16 v[36:51], v[140:143], v[32:35], v[36:51]
	s_nor_b64 s[34:35], s[34:35], s[26:27]
	s_waitcnt lgkmcnt(0)
	v_mfma_f32_32x32x16_f16 v[36:51], v[144:147], v[16:19], v[36:51]
	s_and_saveexec_b64 s[14:15], s[34:35]
	s_cbranch_execz .LBB8_432
	ds_write_b128 v198, v[8:11] offset:16
	s_waitcnt vmcnt(0)
	ds_write_b32 v247, v209 offset:548
	ds_write_b32 v248, v209 offset:536
	ds_write_b32 v249, v209 offset:560

	.amdhsa_kernel _Z8k3t_mfmaILi1EEvPK15HIP_vector_typeIjLj4EEPKjS3_PKfPf
		.amdhsa_group_segment_fixed_size 0
		.amdhsa_private_segment_fixed_size 0
		.amdhsa_kernarg_size 296
		.amdhsa_user_sgpr_count 2
		.amdhsa_user_sgpr_dispatch_ptr 0
		.amdhsa_user_sgpr_queue_ptr 0
		.amdhsa_user_sgpr_kernarg_segment_ptr 1
		.amdhsa_user_sgpr_dispatch_id 0
		.amdhsa_user_sgpr_kernarg_preload_length 0
		.amdhsa_user_sgpr_kernarg_preload_offset 0
		.amdhsa_user_sgpr_private_segment_size 0
		.amdhsa_uses_dynamic_stack 0
		.amdhsa_enable_private_segment 0
		.amdhsa_system_sgpr_workgroup_id_x 1
		.amdhsa_system_sgpr_workgroup_id_y 0
		.amdhsa_system_sgpr_workgroup_id_z 0
		.amdhsa_system_sgpr_workgroup_info 0
		.amdhsa_system_vgpr_workitem_id 0
		.amdhsa_next_free_vgpr 256
		.amdhsa_next_free_sgpr 68
		.amdhsa_accum_offset 256
		.amdhsa_reserve_vcc 1
		.amdhsa_float_round_mode_32 0
		.amdhsa_float_round_mode_16_64 0
		.amdhsa_float_denorm_mode_32 3
		.amdhsa_float_denorm_mode_16_64 3
		.amdhsa_dx10_clamp 1
		.amdhsa_ieee_mode 1
		.amdhsa_fp16_overflow 0
		.amdhsa_tg_split 0
		.amdhsa_exception_fp_ieee_invalid_op 0
		.amdhsa_exception_fp_denorm_src 0
		.amdhsa_exception_fp_ieee_div_zero 0
		.amdhsa_exception_fp_ieee_overflow 0
		.amdhsa_exception_fp_ieee_underflow 0
		.amdhsa_exception_fp_ieee_inexact 0
		.amdhsa_exception_int_div_zero 0
	.end_amdhsa_kernel

amdhsa.kernels:
  - .agpr_count:     0
    .args:
      - .actual_access:  read_only
        .address_space:  global
        .offset:         0
        .size:           8
        .value_kind:     global_buffer
      - .actual_access:  read_only
        .address_space:  global
        .offset:         8
        .size:           8
        .value_kind:     global_buffer
      - .actual_access:  read_only
        .address_space:  global
        .offset:         16
        .size:           8
        .value_kind:     global_buffer
      - .actual_access:  write_only
        .address_space:  global
        .offset:         24
        .size:           8
        .value_kind:     global_buffer
      - .actual_access:  write_only
        .address_space:  global
        .offset:         32
        .size:           8
        .value_kind:     global_buffer
    .group_segment_fixed_size: 6520
    .kernarg_segment_align: 8
    .kernarg_segment_size: 40
    .language:       OpenCL C
    .language_version:
      - 2
      - 0
    .max_flat_workgroup_size: 256
    .name:           _Z8k1_naivePKfS0_S0_P15HIP_vector_typeIjLj4EEPj
    .private_segment_fixed_size: 0
    .sgpr_count:     30
    .sgpr_spill_count: 0
    .symbol:         _Z8k1_naivePKfS0_S0_P15HIP_vector_typeIjLj4EEPj.kd
    .uniform_work_group_size: 1
    .uses_dynamic_stack: false
    .vgpr_count:     40
    .vgpr_spill_count: 0
    .wavefront_size: 64
  - .agpr_count:     0
    .args:
      - .actual_access:  read_only
        .address_space:  global
        .offset:         0
        .size:           8
        .value_kind:     global_buffer
      - .actual_access:  read_only
        .address_space:  global
        .offset:         8
        .size:           8
        .value_kind:     global_buffer
      - .actual_access:  read_only
        .address_space:  global
        .offset:         16
        .size:           8
        .value_kind:     global_buffer
      - .actual_access:  read_only
        .address_space:  global
        .offset:         24
        .size:           8
        .value_kind:     global_buffer
      - .actual_access:  write_only
        .address_space:  global
        .offset:         32
        .size:           8
        .value_kind:     global_buffer
      - .actual_access:  write_only
        .address_space:  global
        .offset:         40
        .size:           8
        .value_kind:     global_buffer
      - .offset:         48
        .size:           4
        .value_kind:     by_value
    .group_segment_fixed_size: 32448
    .kernarg_segment_align: 8
    .kernarg_segment_size: 52
    .language:       OpenCL C
    .language_version:
      - 2
      - 0
    .max_flat_workgroup_size: 256
    .name:           _Z8k2_naivePK15HIP_vector_typeIjLj4EEPKjPKfS6_PS0_Pji
    .private_segment_fixed_size: 0
    .sgpr_count:     30
    .sgpr_spill_count: 0
    .symbol:         _Z8k2_naivePK15HIP_vector_typeIjLj4EEPKjPKfS6_PS0_Pji.kd
    .uniform_work_group_size: 1
    .uses_dynamic_stack: false
    .vgpr_count:     102
    .vgpr_spill_count: 0
    .wavefront_size: 64
  - .agpr_count:     0
    .args:
      - .actual_access:  read_only
        .address_space:  global
        .offset:         0
        .size:           8
        .value_kind:     global_buffer
      - .actual_access:  read_only
        .address_space:  global
        .offset:         8
        .size:           8
        .value_kind:     global_buffer
      - .actual_access:  read_only
        .address_space:  global
        .offset:         16
        .size:           8
        .value_kind:     global_buffer
      - .actual_access:  read_only
        .address_space:  global
        .offset:         24
        .size:           8
        .value_kind:     global_buffer
      - .actual_access:  write_only
        .address_space:  global
        .offset:         32
        .size:           8
        .value_kind:     global_buffer
      - .actual_access:  write_only
        .address_space:  global
        .offset:         40
        .size:           8
        .value_kind:     global_buffer
      - .offset:         48
        .size:           4
        .value_kind:     hidden_block_count_x
      - .offset:         52
        .size:           4
        .value_kind:     hidden_block_count_y
      - .offset:         56
        .size:           4
        .value_kind:     hidden_block_count_z
      - .offset:         60
        .size:           2
        .value_kind:     hidden_group_size_x
      - .offset:         62
        .size:           2
        .value_kind:     hidden_group_size_y
      - .offset:         64
        .size:           2
        .value_kind:     hidden_group_size_z
      - .offset:         66
        .size:           2
        .value_kind:     hidden_remainder_x
      - .offset:         68
        .size:           2
        .value_kind:     hidden_remainder_y
      - .offset:         70
        .size:           2
        .value_kind:     hidden_remainder_z
      - .offset:         88
        .size:           8
        .value_kind:     hidden_global_offset_x
      - .offset:         96
        .size:           8
        .value_kind:     hidden_global_offset_y
      - .offset:         104
        .size:           8
        .value_kind:     hidden_global_offset_z
      - .offset:         112
        .size:           2
        .value_kind:     hidden_grid_dims
      - .offset:         168
        .size:           4
        .value_kind:     hidden_dynamic_lds_size
    .group_segment_fixed_size: 0
    .kernarg_segment_align: 8
    .kernarg_segment_size: 304
    .language:       OpenCL C
    .language_version:
      - 2
      - 0
    .max_flat_workgroup_size: 512
    .name:           _Z7k2_mfmaPK15HIP_vector_typeIjLj4EEPKjS2_PKfPS0_Pj
    .private_segment_fixed_size: 0
    .sgpr_count:     52
    .sgpr_spill_count: 0
    .symbol:         _Z7k2_mfmaPK15HIP_vector_typeIjLj4EEPKjS2_PKfPS0_Pj.kd
    .uniform_work_group_size: 1
    .uses_dynamic_stack: false
    .vgpr_count:     256
    .vgpr_spill_count: 0
    .wavefront_size: 64
  - .agpr_count:     0
    .args:
      - .actual_access:  read_only
        .address_space:  global
        .offset:         0
        .size:           8
        .value_kind:     global_buffer
      - .actual_access:  write_only
        .address_space:  global
        .offset:         8
        .size:           8
        .value_kind:     global_buffer
      - .offset:         16
        .size:           4
        .value_kind:     hidden_block_count_x
      - .offset:         20
        .size:           4
        .value_kind:     hidden_block_count_y
      - .offset:         24
        .size:           4
        .value_kind:     hidden_block_count_z
      - .offset:         28
        .size:           2
        .value_kind:     hidden_group_size_x
      - .offset:         30
        .size:           2
        .value_kind:     hidden_group_size_y
      - .offset:         32
        .size:           2
        .value_kind:     hidden_group_size_z
      - .offset:         34
        .size:           2
        .value_kind:     hidden_remainder_x
      - .offset:         36
        .size:           2
        .value_kind:     hidden_remainder_y
      - .offset:         38
        .size:           2
        .value_kind:     hidden_remainder_z
      - .offset:         56
        .size:           8
        .value_kind:     hidden_global_offset_x
      - .offset:         64
        .size:           8
        .value_kind:     hidden_global_offset_y
      - .offset:         72
        .size:           8
        .value_kind:     hidden_global_offset_z
      - .offset:         80
        .size:           2
        .value_kind:     hidden_grid_dims
    .group_segment_fixed_size: 0
    .kernarg_segment_align: 8
    .kernarg_segment_size: 272
    .language:       OpenCL C
    .language_version:
      - 2
      - 0
    .max_flat_workgroup_size: 1024
    .name:           _Z7prep_w3PKfP15HIP_vector_typeIjLj4EE
    .private_segment_fixed_size: 0
    .sgpr_count:     18
    .sgpr_spill_count: 0
    .symbol:         _Z7prep_w3PKfP15HIP_vector_typeIjLj4EE.kd
    .uniform_work_group_size: 1
    .uses_dynamic_stack: false
    .vgpr_count:     13
    .vgpr_spill_count: 0
    .wavefront_size: 64
  - .agpr_count:     0
    .args:
      - .actual_access:  read_only
        .address_space:  global
        .offset:         0
        .size:           8
        .value_kind:     global_buffer
      - .actual_access:  read_only
        .address_space:  global
        .offset:         8
        .size:           8
        .value_kind:     global_buffer
      - .actual_access:  read_only
        .address_space:  global
        .offset:         16
        .size:           8
        .value_kind:     global_buffer
      - .actual_access:  read_only
        .address_space:  global
        .offset:         24
        .size:           8
        .value_kind:     global_buffer
      - .address_space:  global
        .offset:         32
        .size:           8
        .value_kind:     global_buffer
      - .offset:         40
        .size:           4
        .value_kind:     by_value
      - .offset:         48
        .size:           4
        .value_kind:     hidden_block_count_x
      - .offset:         52
        .size:           4
        .value_kind:     hidden_block_count_y
      - .offset:         56
        .size:           4
        .value_kind:     hidden_block_count_z
      - .offset:         60
        .size:           2
        .value_kind:     hidden_group_size_x
      - .offset:         62
        .size:           2
        .value_kind:     hidden_group_size_y
      - .offset:         64
        .size:           2
        .value_kind:     hidden_group_size_z
      - .offset:         66
        .size:           2
        .value_kind:     hidden_remainder_x
      - .offset:         68
        .size:           2
        .value_kind:     hidden_remainder_y
      - .offset:         70
        .size:           2
        .value_kind:     hidden_remainder_z
      - .offset:         88
        .size:           8
        .value_kind:     hidden_global_offset_x
      - .offset:         96
        .size:           8
        .value_kind:     hidden_global_offset_y
      - .offset:         104
        .size:           8
        .value_kind:     hidden_global_offset_z
      - .offset:         112
        .size:           2
        .value_kind:     hidden_grid_dims
    .group_segment_fixed_size: 25344
    .kernarg_segment_align: 8
    .kernarg_segment_size: 304
    .language:       OpenCL C
    .language_version:
      - 2
      - 0
    .max_flat_workgroup_size: 64
    .name:           _Z7k3_mfmaPK15HIP_vector_typeIjLj4EEPKjS2_PKfPfi
    .private_segment_fixed_size: 0
    .sgpr_count:     52
    .sgpr_spill_count: 0
    .symbol:         _Z7k3_mfmaPK15HIP_vector_typeIjLj4EEPKjS2_PKfPfi.kd
    .uniform_work_group_size: 1
    .uses_dynamic_stack: false
    .vgpr_count:     192
    .vgpr_spill_count: 0
    .wavefront_size: 64
  - .agpr_count:     0
    .args:
      - .actual_access:  read_only
        .address_space:  global
        .offset:         0
        .size:           8
        .value_kind:     global_buffer
      - .actual_access:  read_only
        .address_space:  global
        .offset:         8
        .size:           8
        .value_kind:     global_buffer
      - .actual_access:  read_only
        .address_space:  global
        .offset:         16
        .size:           8
        .value_kind:     global_buffer
      - .actual_access:  write_only
        .address_space:  global
        .offset:         24
        .size:           8
        .value_kind:     global_buffer
      - .actual_access:  write_only
        .address_space:  global
        .offset:         32
        .size:           8
        .value_kind:     global_buffer
      - .actual_access:  read_only
        .address_space:  global
        .offset:         40
        .size:           8
        .value_kind:     global_buffer
      - .actual_access:  read_only
        .address_space:  global
        .offset:         48
        .size:           8
        .value_kind:     global_buffer
      - .actual_access:  read_only
        .address_space:  global
        .offset:         56
        .size:           8
        .value_kind:     global_buffer
      - .actual_access:  write_only
        .address_space:  global
        .offset:         64
        .size:           8
        .value_kind:     global_buffer
      - .actual_access:  write_only
        .address_space:  global
        .offset:         72
        .size:           8
        .value_kind:     global_buffer
    .group_segment_fixed_size: 62848
    .kernarg_segment_align: 8
    .kernarg_segment_size: 80
    .language:       OpenCL C
    .language_version:
      - 2
      - 0
    .max_flat_workgroup_size: 256
    .name:           _Z7k1_mfmaPKfS0_S0_P15HIP_vector_typeIjLj4EEPjS0_S0_S0_S3_S3_
    .private_segment_fixed_size: 0
    .sgpr_count:     28
    .sgpr_spill_count: 0
    .symbol:         _Z7k1_mfmaPKfS0_S0_P15HIP_vector_typeIjLj4EEPjS0_S0_S0_S3_S3_.kd
    .uniform_work_group_size: 1
    .uses_dynamic_stack: false
    .vgpr_count:     170
    .vgpr_spill_count: 0
    .wavefront_size: 64
  - .agpr_count:     0
    .args:
      - .actual_access:  read_only
        .address_space:  global
        .offset:         0
        .size:           8
        .value_kind:     global_buffer
      - .actual_access:  read_only
        .address_space:  global
        .offset:         8
        .size:           8
        .value_kind:     global_buffer
      - .actual_access:  read_only
        .address_space:  global
        .offset:         16
        .size:           8
        .value_kind:     global_buffer
      - .actual_access:  read_only
        .address_space:  global
        .offset:         24
        .size:           8
        .value_kind:     global_buffer
      - .actual_access:  write_only
        .address_space:  global
        .offset:         32
        .size:           8
        .value_kind:     global_buffer
      - .actual_access:  write_only
        .address_space:  global
        .offset:         40
        .size:           8
        .value_kind:     global_buffer
      - .actual_access:  read_only
        .address_space:  global
        .offset:         48
        .size:           8
        .value_kind:     global_buffer
      - .actual_access:  read_only
        .address_space:  global
        .offset:         56
        .size:           8
        .value_kind:     global_buffer
      - .actual_access:  read_only
        .address_space:  global
        .offset:         64
        .size:           8
        .value_kind:     global_buffer
      - .actual_access:  read_only
        .address_space:  global
        .offset:         72
        .size:           8
        .value_kind:     global_buffer
      - .actual_access:  write_only
        .address_space:  global
        .offset:         80
        .size:           8
        .value_kind:     global_buffer
    .group_segment_fixed_size: 0
    .kernarg_segment_align: 8
    .kernarg_segment_size: 88
    .language:       OpenCL C
    .language_version:
      - 2
      - 0
    .max_flat_workgroup_size: 512
    .name:           _Z8k23_mfmaPK15HIP_vector_typeIjLj4EEPKjS2_PKfPS0_PjS2_S4_S2_S6_Pf
    .private_segment_fixed_size: 0
    .sgpr_count:     76
    .sgpr_spill_count: 0
    .symbol:         _Z8k23_mfmaPK15HIP_vector_typeIjLj4EEPKjS2_PKfPS0_PjS2_S4_S2_S6_Pf.kd
    .uniform_work_group_size: 1
    .uses_dynamic_stack: false
    .vgpr_count:     256
    .vgpr_spill_count: 0
    .wavefront_size: 64
  - .agpr_count:     0
    .args:
      - .actual_access:  read_only
        .address_space:  global
        .offset:         0
        .size:           8
        .value_kind:     global_buffer
      - .actual_access:  read_only
        .address_space:  global
        .offset:         8
        .size:           8
        .value_kind:     global_buffer
      - .actual_access:  read_only
        .address_space:  global
        .offset:         16
        .size:           8
        .value_kind:     global_buffer
      - .actual_access:  read_only
        .address_space:  global
        .offset:         24
        .size:           8
        .value_kind:     global_buffer
      - .address_space:  global
        .offset:         32
        .size:           8
        .value_kind:     global_buffer
      - .offset:         40
        .size:           4
        .value_kind:     by_value
    .group_segment_fixed_size: 3240
    .kernarg_segment_align: 8
    .kernarg_segment_size: 44
    .language:       OpenCL C
    .language_version:
      - 2
      - 0
    .max_flat_workgroup_size: 256
    .name:           _Z8k3_naivePK15HIP_vector_typeIjLj4EEPKjPKfS6_Pfi
    .private_segment_fixed_size: 0
    .sgpr_count:     28
    .sgpr_spill_count: 0
    .symbol:         _Z8k3_naivePK15HIP_vector_typeIjLj4EEPKjPKfS6_Pfi.kd
    .uniform_work_group_size: 1
    .uses_dynamic_stack: false
    .vgpr_count:     32
    .vgpr_spill_count: 0
    .wavefront_size: 64
  - .agpr_count:     0
    .args:
      - .actual_access:  read_only
        .address_space:  global
        .offset:         0
        .size:           8
        .value_kind:     global_buffer
      - .actual_access:  read_only
        .address_space:  global
        .offset:         8
        .size:           8
        .value_kind:     global_buffer
      - .actual_access:  read_only
        .address_space:  global
        .offset:         16
        .size:           8
        .value_kind:     global_buffer
      - .actual_access:  read_only
        .address_space:  global
        .offset:         24
        .size:           8
        .value_kind:     global_buffer
      - .address_space:  global
        .offset:         32
        .size:           8
        .value_kind:     global_buffer
      - .offset:         40
        .size:           4
        .value_kind:     hidden_block_count_x
      - .offset:         44
        .size:           4
        .value_kind:     hidden_block_count_y
      - .offset:         48
        .size:           4
        .value_kind:     hidden_block_count_z
      - .offset:         52
        .size:           2
        .value_kind:     hidden_group_size_x
      - .offset:         54
        .size:           2
        .value_kind:     hidden_group_size_y
      - .offset:         56
        .size:           2
        .value_kind:     hidden_group_size_z
      - .offset:         58
        .size:           2
        .value_kind:     hidden_remainder_x
      - .offset:         60
        .size:           2
        .value_kind:     hidden_remainder_y
      - .offset:         62
        .size:           2
        .value_kind:     hidden_remainder_z
      - .offset:         80
        .size:           8
        .value_kind:     hidden_global_offset_x
      - .offset:         88
        .size:           8
        .value_kind:     hidden_global_offset_y
      - .offset:         96
        .size:           8
        .value_kind:     hidden_global_offset_z
      - .offset:         104
        .size:           2
        .value_kind:     hidden_grid_dims
      - .offset:         160
        .size:           4
        .value_kind:     hidden_dynamic_lds_size
    .group_segment_fixed_size: 0
    .kernarg_segment_align: 8
    .kernarg_segment_size: 296
    .language:       OpenCL C
    .language_version:
      - 2
      - 0
    .max_flat_workgroup_size: 512
    .name:           _Z8k3t_mfmaILi1EEvPK15HIP_vector_typeIjLj4EEPKjS3_PKfPf
    .private_segment_fixed_size: 0
    .sgpr_count:     74
    .sgpr_spill_count: 0
    .symbol:         _Z8k3t_mfmaILi1EEvPK15HIP_vector_typeIjLj4EEPKjS3_PKfPf.kd
    .uniform_work_group_size: 1
    .uses_dynamic_stack: false
    .vgpr_count:     256
    .vgpr_spill_count: 0
    .wavefront_size: 64
